# speedup vs baseline: 1.0168x; 1.0047x over previous
_Z5k_decPKiPKDF16_S2_PKfS4_S4_Pf:
	s_load_dword s3, s[0:1], 0x44
	s_load_dword s6, s[0:1], 0x38
	s_load_dwordx2 s[4:5], s[0:1], 0x0
	s_load_dwordx8 s[28:35], s[0:1], 0x8
	s_load_dwordx4 s[12:15], s[0:1], 0x28
	v_and_b32_e32 v1, 15, v0
	v_and_b32_e32 v64, 63, v0
	v_lshlrev_b32_e32 v96, 3, v1
	v_lshrrev_b32_e32 v4, 3, v0
	v_and_b32_e32 v4, 4, v4
	v_or_b32_e32 v96, v96, v4
	v_mov_b32_e32 v97, 0
	v_and_b32_e32 v104, 16, v0
	v_lshlrev_b32_e32 v6, 7, v0
	v_lshlrev_b32_e32 v7, 2, v64
	s_movk_i32 s16, 0x6000
	v_and_or_b32 v103, v6, s16, v7
	v_mov_b32_e32 v219, 0
	s_movk_i32 s19, 0x3d08
	s_waitcnt lgkmcnt(0)
	s_and_b32 s3, s3, 0xffff
	s_mul_i32 s2, s2, s3
	v_add_u32_e32 v5, s2, v0
	s_mul_i32 s6, s6, s3
	v_lshrrev_b32_e32 v102, 6, v5
	s_lshr_b32 s18, s6, 6
	v_readfirstlane_b32 s23, v102
	v_lshl_add_u64 v[2:3], s[4:5], 0, v[96:97]
	s_mov_b32 s16, 0xf4240
	v_cmp_gt_u32_e32 vcc, s16, v5
	s_and_saveexec_b64 s[22:23], vcc
	s_cbranch_execz .LBB2_3
	v_mov_b32_e32 v222, v2
	v_mov_b32_e32 v223, v3
	v_min_u32_e32 v218, s19, v102
	v_lshlrev_b32_e32 v218, 9, v218
	v_lshl_add_u64 v[216:217], v[222:223], 0, v[218:219]
	global_load_dword v65, v[216:217], off nt
	global_load_dword v80, v[216:217], off offset:128 nt
	global_load_dword v81, v[216:217], off offset:256 nt
	global_load_dword v82, v[216:217], off offset:384 nt
	v_add_u32_e32 v220, s18, v102
	v_min_u32_e32 v218, s19, v220
	v_lshlrev_b32_e32 v218, 9, v218
	v_lshl_add_u64 v[216:217], v[222:223], 0, v[218:219]
	global_load_dword v100, v[216:217], off nt
	global_load_dword v101, v[216:217], off offset:128 nt
	global_load_dword v98, v[216:217], off offset:256 nt
	global_load_dword v99, v[216:217], off offset:384 nt
	s_mov_b32 s8, s28
	s_and_b32 s9, s29, 0xffff
	s_mov_b32 s10, 0x30d400
	s_mov_b32 s11, 0x20000
	s_mov_b64 s[36:37], 0x1000
	v_and_b32_e32 v96, 48, v64
	v_lshlrev_b32_e32 v221, 6, v1
	v_lshlrev_b32_e32 v211, 2, v1
	v_mov_b32_e32 v214, v221
	v_mov_b32_e32 v215, 0
	v_lshl_add_u64 v[216:217], s[30:31], 0, v[96:97]
	v_lshl_add_u64 v[48:49], v[216:217], 0, v[214:215]
	v_lshl_add_u64 v[66:67], v[48:49], 0, s[36:37]
	v_lshl_or_b32 v221, v102, 6, v64
	v_lshrrev_b32_e32 v213, 4, v64
	v_cmp_gt_u32_e32 vcc, 16, v64
	v_and_b32_e32 v210, 31, v64
	v_lshlrev_b32_e32 v210, 4, v210
	s_mov_b32 s38, -1
	s_mov_b32 s39, 0
	s_mov_b64 exec, s[38:39]
	global_load_dwordx4 v[126:129], v210, s[32:33]
	s_mov_b32 s38, 0
	s_mov_b32 s39, -1
	s_mov_b64 exec, s[38:39]
	global_load_dwordx4 v[126:129], v210, s[34:35]
	s_mov_b64 exec, -1
	global_load_dwordx4 v[32:35], v[48:49], off
	global_load_dwordx4 v[36:39], v[48:49], off offset:1024
	global_load_dwordx4 v[40:43], v[48:49], off offset:2048
	global_load_dwordx4 v[44:47], v[48:49], off offset:3072
	s_nop 0
	global_load_dwordx4 v[48:51], v[66:67], off
	global_load_dwordx4 v[52:55], v[66:67], off offset:1024
	global_load_dwordx4 v[56:59], v[66:67], off offset:2048
	global_load_dwordx4 v[60:63], v[66:67], off offset:3072
	s_load_dword s12, s[12:13], 0x0
	s_waitcnt vmcnt(14)
	v_lshl_or_b32 v216, v65, 5, v104
	v_lshl_or_b32 v217, v80, 5, v104
	v_lshl_or_b32 v218, v81, 5, v104
	v_lshl_or_b32 v212, v82, 5, v104
	buffer_load_dwordx4 v[92:95], v216, s[8:11], 0 offen
	buffer_load_dwordx4 v[88:91], v217, s[8:11], 0 offen
	buffer_load_dwordx4 v[84:87], v218, s[8:11], 0 offen
	buffer_load_dwordx4 v[80:83], v212, s[8:11], 0 offen
	s_lshl_b32 s21, s18, 6
	s_mov_b32 s20, 2
	s_mov_b64 s[16:17], 0
	v_cmp_eq_u32_e64 s[0:1], 1, v213
	v_cmp_eq_u32_e64 s[2:3], 2, v213
	v_cmp_eq_u32_e64 s[4:5], 3, v213
	v_mov_b32_e32 v96, v221
	v_mov_b32_e32 v97, 0
	s_waitcnt vmcnt(4)
	v_lshrrev_b32_e32 v210, 6, v0
	v_lshlrev_b32_e32 v210, 10, v210
	v_add_u32_e32 v210, 0x8000, v210
	v_lshl_add_u32 v130, v64, 4, v210
	v_lshl_add_u32 v131, v213, 4, v210
	v_add_u32_e32 v132, v211, v210
	ds_write_b128 v130, v[126:129]
	ds_read_b128 v[68:71], v131 offset:512
	ds_read_b128 v[72:75], v131 offset:576
	ds_read_b128 v[76:79], v131 offset:640
	ds_read_b128 v[106:109], v131 offset:704
	ds_read_b128 v[110:113], v131 offset:768
	ds_read_b128 v[114:117], v131 offset:832
	ds_read_b128 v[118:121], v131 offset:896
	ds_read_b128 v[122:125], v131 offset:960
	s_waitcnt lgkmcnt(0)
	ds_read_b32 v148, v132 offset:512
	ds_read_b32 v149, v132 offset:576
	ds_read_b32 v150, v132 offset:640
	ds_read_b32 v151, v132 offset:704
	ds_read_b32 v152, v132 offset:768
	ds_read_b32 v153, v132 offset:832
	ds_read_b32 v154, v132 offset:896
	ds_read_b32 v155, v132 offset:960
	ds_read_b32 v156, v132 offset:0
	ds_read_b32 v157, v132 offset:64
	ds_read_b32 v158, v132 offset:128
	ds_read_b32 v159, v132 offset:192
	s_waitcnt lgkmcnt(0)
	ds_read_b32 v160, v132 offset:256
	ds_read_b32 v161, v132 offset:320
	ds_read_b32 v162, v132 offset:384
	ds_read_b32 v163, v132 offset:448
	ds_read_b128 v[0:3], v131 offset:0
	ds_read_b128 v[4:7], v131 offset:64
	ds_read_b128 v[8:11], v131 offset:128
	ds_read_b128 v[12:15], v131 offset:192
	ds_read_b128 v[16:19], v131 offset:256
	ds_read_b128 v[20:23], v131 offset:320
	ds_read_b128 v[24:27], v131 offset:384
	ds_read_b128 v[28:31], v131 offset:448
	s_waitcnt lgkmcnt(0)
	v_cvt_pk_f16_f32 v67, v74, v75
	v_cvt_pk_f16_f32 v66, v72, v73
	v_cvt_pk_f16_f32 v65, v70, v71
	v_cvt_pk_f16_f32 v64, v68, v69
	v_cvt_pk_f16_f32 v71, v108, v109
	v_cvt_pk_f16_f32 v70, v106, v107
	v_cvt_pk_f16_f32 v69, v78, v79
	v_cvt_pk_f16_f32 v68, v76, v77
	v_cvt_pk_f16_f32 v75, v116, v117
	v_cvt_pk_f16_f32 v74, v114, v115
	v_cvt_pk_f16_f32 v73, v112, v113
	v_cvt_pk_f16_f32 v72, v110, v111
	v_cvt_pk_f16_f32 v79, v124, v125
	v_cvt_pk_f16_f32 v78, v122, v123
	v_cvt_pk_f16_f32 v77, v120, v121
	v_cvt_pk_f16_f32 v76, v118, v119
	v_mov_b32_e32 v167, 0x38003800
	v_pk_mul_f16 v64, v64, v167
	v_pk_mul_f16 v65, v65, v167
	v_pk_mul_f16 v66, v66, v167
	v_pk_mul_f16 v67, v67, v167
	v_pk_mul_f16 v68, v68, v167
	v_pk_mul_f16 v69, v69, v167
	v_pk_mul_f16 v70, v70, v167
	v_pk_mul_f16 v71, v71, v167
	v_pk_mul_f16 v72, v72, v167
	v_pk_mul_f16 v73, v73, v167
	v_pk_mul_f16 v74, v74, v167
	v_pk_mul_f16 v75, v75, v167
	v_pk_mul_f16 v76, v76, v167
	v_pk_mul_f16 v77, v77, v167
	v_pk_mul_f16 v78, v78, v167
	v_pk_mul_f16 v79, v79, v167
	v_cvt_f16_f32_e32 v148, v148
	v_cvt_f16_f32_e32 v149, v149
	v_cvt_f16_f32_e32 v150, v150
	v_cvt_f16_f32_e32 v151, v151
	v_cvt_f16_f32_e32 v152, v152
	v_cvt_f16_f32_e32 v153, v153
	v_cvt_f16_f32_e32 v154, v154
	v_cvt_f16_f32_e32 v155, v155
	v_cvt_f32_f16_e32 v148, v148
	v_cvt_f32_f16_e32 v149, v149
	v_cvt_f32_f16_e32 v150, v150
	v_cvt_f32_f16_e32 v151, v151
	v_cvt_f32_f16_e32 v152, v152
	v_cvt_f32_f16_e32 v153, v153
	v_cvt_f32_f16_e32 v154, v154
	v_cvt_f32_f16_e32 v155, v155
	v_mul_f32_e32 v148, 0.5, v148
	v_mul_f32_e32 v149, 0.5, v149
	v_mul_f32_e32 v150, 0.5, v150
	v_mul_f32_e32 v151, 0.5, v151
	v_mul_f32_e32 v152, 0.5, v152
	v_mul_f32_e32 v153, 0.5, v153
	v_mul_f32_e32 v154, 0.5, v154
	v_mul_f32_e32 v155, 0.5, v155
	v_mov_b32_e32 v140, 0
	v_mov_b32_e32 v141, 0
	v_mov_b32_e32 v142, 0
	v_mov_b32_e32 v143, 0
	v_mov_b32_e32 v144, 0
	v_mov_b32_e32 v145, 0
	v_mov_b32_e32 v146, 0
	v_mov_b32_e32 v147, 0
	v_mov_b32_e32 v166, 0
	v_cvt_f32_f16_e32 v164, v32
	v_cvt_f32_f16_sdwa v165, v32 dst_sel:DWORD dst_unused:UNUSED_PAD src0_sel:WORD_1
	v_fmac_f32_e32 v140, v148, v164
	v_fmac_f32_e32 v141, v148, v165
	v_cvt_f32_f16_e32 v164, v33
	v_cvt_f32_f16_sdwa v165, v33 dst_sel:DWORD dst_unused:UNUSED_PAD src0_sel:WORD_1
	v_fmac_f32_e32 v142, v148, v164
	v_fmac_f32_e32 v143, v148, v165
	v_cvt_f32_f16_e32 v164, v34
	v_cvt_f32_f16_sdwa v165, v34 dst_sel:DWORD dst_unused:UNUSED_PAD src0_sel:WORD_1
	v_fmac_f32_e32 v144, v148, v164
	v_fmac_f32_e32 v145, v148, v165
	v_cvt_f32_f16_e32 v164, v35
	v_cvt_f32_f16_sdwa v165, v35 dst_sel:DWORD dst_unused:UNUSED_PAD src0_sel:WORD_1
	v_fmac_f32_e32 v146, v148, v164
	v_fmac_f32_e32 v147, v148, v165
	v_fmac_f32_e32 v166, v148, v156
	v_cvt_f32_f16_e32 v164, v36
	v_cvt_f32_f16_sdwa v165, v36 dst_sel:DWORD dst_unused:UNUSED_PAD src0_sel:WORD_1
	v_fmac_f32_e32 v140, v149, v164
	v_fmac_f32_e32 v141, v149, v165
	v_cvt_f32_f16_e32 v164, v37
	v_cvt_f32_f16_sdwa v165, v37 dst_sel:DWORD dst_unused:UNUSED_PAD src0_sel:WORD_1
	v_fmac_f32_e32 v142, v149, v164
	v_fmac_f32_e32 v143, v149, v165
	v_cvt_f32_f16_e32 v164, v38
	v_cvt_f32_f16_sdwa v165, v38 dst_sel:DWORD dst_unused:UNUSED_PAD src0_sel:WORD_1
	v_fmac_f32_e32 v144, v149, v164
	v_fmac_f32_e32 v145, v149, v165
	v_cvt_f32_f16_e32 v164, v39
	v_cvt_f32_f16_sdwa v165, v39 dst_sel:DWORD dst_unused:UNUSED_PAD src0_sel:WORD_1
	v_fmac_f32_e32 v146, v149, v164
	v_fmac_f32_e32 v147, v149, v165
	v_fmac_f32_e32 v166, v149, v157
	v_cvt_f32_f16_e32 v164, v40
	v_cvt_f32_f16_sdwa v165, v40 dst_sel:DWORD dst_unused:UNUSED_PAD src0_sel:WORD_1
	v_fmac_f32_e32 v140, v150, v164
	v_fmac_f32_e32 v141, v150, v165
	v_cvt_f32_f16_e32 v164, v41
	v_cvt_f32_f16_sdwa v165, v41 dst_sel:DWORD dst_unused:UNUSED_PAD src0_sel:WORD_1
	v_fmac_f32_e32 v142, v150, v164
	v_fmac_f32_e32 v143, v150, v165
	v_cvt_f32_f16_e32 v164, v42
	v_cvt_f32_f16_sdwa v165, v42 dst_sel:DWORD dst_unused:UNUSED_PAD src0_sel:WORD_1
	v_fmac_f32_e32 v144, v150, v164
	v_fmac_f32_e32 v145, v150, v165
	v_cvt_f32_f16_e32 v164, v43
	v_cvt_f32_f16_sdwa v165, v43 dst_sel:DWORD dst_unused:UNUSED_PAD src0_sel:WORD_1
	v_fmac_f32_e32 v146, v150, v164
	v_fmac_f32_e32 v147, v150, v165
	v_fmac_f32_e32 v166, v150, v158
	v_cvt_f32_f16_e32 v164, v44
	v_cvt_f32_f16_sdwa v165, v44 dst_sel:DWORD dst_unused:UNUSED_PAD src0_sel:WORD_1
	v_fmac_f32_e32 v140, v151, v164
	v_fmac_f32_e32 v141, v151, v165
	v_cvt_f32_f16_e32 v164, v45
	v_cvt_f32_f16_sdwa v165, v45 dst_sel:DWORD dst_unused:UNUSED_PAD src0_sel:WORD_1
	v_fmac_f32_e32 v142, v151, v164
	v_fmac_f32_e32 v143, v151, v165
	v_cvt_f32_f16_e32 v164, v46
	v_cvt_f32_f16_sdwa v165, v46 dst_sel:DWORD dst_unused:UNUSED_PAD src0_sel:WORD_1
	v_fmac_f32_e32 v144, v151, v164
	v_fmac_f32_e32 v145, v151, v165
	v_cvt_f32_f16_e32 v164, v47
	v_cvt_f32_f16_sdwa v165, v47 dst_sel:DWORD dst_unused:UNUSED_PAD src0_sel:WORD_1
	v_fmac_f32_e32 v146, v151, v164
	v_fmac_f32_e32 v147, v151, v165
	v_fmac_f32_e32 v166, v151, v159
	v_cvt_f32_f16_e32 v164, v48
	v_cvt_f32_f16_sdwa v165, v48 dst_sel:DWORD dst_unused:UNUSED_PAD src0_sel:WORD_1
	v_fmac_f32_e32 v140, v152, v164
	v_fmac_f32_e32 v141, v152, v165
	v_cvt_f32_f16_e32 v164, v49
	v_cvt_f32_f16_sdwa v165, v49 dst_sel:DWORD dst_unused:UNUSED_PAD src0_sel:WORD_1
	v_fmac_f32_e32 v142, v152, v164
	v_fmac_f32_e32 v143, v152, v165
	v_cvt_f32_f16_e32 v164, v50
	v_cvt_f32_f16_sdwa v165, v50 dst_sel:DWORD dst_unused:UNUSED_PAD src0_sel:WORD_1
	v_fmac_f32_e32 v144, v152, v164
	v_fmac_f32_e32 v145, v152, v165
	v_cvt_f32_f16_e32 v164, v51
	v_cvt_f32_f16_sdwa v165, v51 dst_sel:DWORD dst_unused:UNUSED_PAD src0_sel:WORD_1
	v_fmac_f32_e32 v146, v152, v164
	v_fmac_f32_e32 v147, v152, v165
	v_fmac_f32_e32 v166, v152, v160
	v_cvt_f32_f16_e32 v164, v52
	v_cvt_f32_f16_sdwa v165, v52 dst_sel:DWORD dst_unused:UNUSED_PAD src0_sel:WORD_1
	v_fmac_f32_e32 v140, v153, v164
	v_fmac_f32_e32 v141, v153, v165
	v_cvt_f32_f16_e32 v164, v53
	v_cvt_f32_f16_sdwa v165, v53 dst_sel:DWORD dst_unused:UNUSED_PAD src0_sel:WORD_1
	v_fmac_f32_e32 v142, v153, v164
	v_fmac_f32_e32 v143, v153, v165
	v_cvt_f32_f16_e32 v164, v54
	v_cvt_f32_f16_sdwa v165, v54 dst_sel:DWORD dst_unused:UNUSED_PAD src0_sel:WORD_1
	v_fmac_f32_e32 v144, v153, v164
	v_fmac_f32_e32 v145, v153, v165
	v_cvt_f32_f16_e32 v164, v55
	v_cvt_f32_f16_sdwa v165, v55 dst_sel:DWORD dst_unused:UNUSED_PAD src0_sel:WORD_1
	v_fmac_f32_e32 v146, v153, v164
	v_fmac_f32_e32 v147, v153, v165
	v_fmac_f32_e32 v166, v153, v161
	v_cvt_f32_f16_e32 v164, v56
	v_cvt_f32_f16_sdwa v165, v56 dst_sel:DWORD dst_unused:UNUSED_PAD src0_sel:WORD_1
	v_fmac_f32_e32 v140, v154, v164
	v_fmac_f32_e32 v141, v154, v165
	v_cvt_f32_f16_e32 v164, v57
	v_cvt_f32_f16_sdwa v165, v57 dst_sel:DWORD dst_unused:UNUSED_PAD src0_sel:WORD_1
	v_fmac_f32_e32 v142, v154, v164
	v_fmac_f32_e32 v143, v154, v165
	v_cvt_f32_f16_e32 v164, v58
	v_cvt_f32_f16_sdwa v165, v58 dst_sel:DWORD dst_unused:UNUSED_PAD src0_sel:WORD_1
	v_fmac_f32_e32 v144, v154, v164
	v_fmac_f32_e32 v145, v154, v165
	v_cvt_f32_f16_e32 v164, v59
	v_cvt_f32_f16_sdwa v165, v59 dst_sel:DWORD dst_unused:UNUSED_PAD src0_sel:WORD_1
	v_fmac_f32_e32 v146, v154, v164
	v_fmac_f32_e32 v147, v154, v165
	v_fmac_f32_e32 v166, v154, v162
	v_cvt_f32_f16_e32 v164, v60
	v_cvt_f32_f16_sdwa v165, v60 dst_sel:DWORD dst_unused:UNUSED_PAD src0_sel:WORD_1
	v_fmac_f32_e32 v140, v155, v164
	v_fmac_f32_e32 v141, v155, v165
	v_cvt_f32_f16_e32 v164, v61
	v_cvt_f32_f16_sdwa v165, v61 dst_sel:DWORD dst_unused:UNUSED_PAD src0_sel:WORD_1
	v_fmac_f32_e32 v142, v155, v164
	v_fmac_f32_e32 v143, v155, v165
	v_cvt_f32_f16_e32 v164, v62
	v_cvt_f32_f16_sdwa v165, v62 dst_sel:DWORD dst_unused:UNUSED_PAD src0_sel:WORD_1
	v_fmac_f32_e32 v144, v155, v164
	v_fmac_f32_e32 v145, v155, v165
	v_cvt_f32_f16_e32 v164, v63
	v_cvt_f32_f16_sdwa v165, v63 dst_sel:DWORD dst_unused:UNUSED_PAD src0_sel:WORD_1
	v_fmac_f32_e32 v146, v155, v164
	v_fmac_f32_e32 v147, v155, v165
	v_fmac_f32_e32 v166, v155, v163
	v_add_f32_dpp v140, v140, v140 row_ror:8 row_mask:0xf bank_mask:0xf
	v_add_f32_dpp v141, v141, v141 row_ror:8 row_mask:0xf bank_mask:0xf
	v_add_f32_dpp v142, v142, v142 row_ror:8 row_mask:0xf bank_mask:0xf
	v_add_f32_dpp v143, v143, v143 row_ror:8 row_mask:0xf bank_mask:0xf
	v_add_f32_dpp v144, v144, v144 row_ror:8 row_mask:0xf bank_mask:0xf
	v_add_f32_dpp v145, v145, v145 row_ror:8 row_mask:0xf bank_mask:0xf
	v_add_f32_dpp v146, v146, v146 row_ror:8 row_mask:0xf bank_mask:0xf
	v_add_f32_dpp v147, v147, v147 row_ror:8 row_mask:0xf bank_mask:0xf
	v_add_f32_dpp v166, v166, v166 row_ror:8 row_mask:0xf bank_mask:0xf
	v_add_f32_dpp v140, v140, v140 row_ror:4 row_mask:0xf bank_mask:0xf
	v_add_f32_dpp v141, v141, v141 row_ror:4 row_mask:0xf bank_mask:0xf
	v_add_f32_dpp v142, v142, v142 row_ror:4 row_mask:0xf bank_mask:0xf
	v_add_f32_dpp v143, v143, v143 row_ror:4 row_mask:0xf bank_mask:0xf
	v_add_f32_dpp v144, v144, v144 row_ror:4 row_mask:0xf bank_mask:0xf
	v_add_f32_dpp v145, v145, v145 row_ror:4 row_mask:0xf bank_mask:0xf
	v_add_f32_dpp v146, v146, v146 row_ror:4 row_mask:0xf bank_mask:0xf
	v_add_f32_dpp v147, v147, v147 row_ror:4 row_mask:0xf bank_mask:0xf
	v_add_f32_dpp v166, v166, v166 row_ror:4 row_mask:0xf bank_mask:0xf
	v_add_f32_dpp v140, v140, v140 row_ror:2 row_mask:0xf bank_mask:0xf
	v_add_f32_dpp v141, v141, v141 row_ror:2 row_mask:0xf bank_mask:0xf
	v_add_f32_dpp v142, v142, v142 row_ror:2 row_mask:0xf bank_mask:0xf
	v_add_f32_dpp v143, v143, v143 row_ror:2 row_mask:0xf bank_mask:0xf
	v_add_f32_dpp v144, v144, v144 row_ror:2 row_mask:0xf bank_mask:0xf
	v_add_f32_dpp v145, v145, v145 row_ror:2 row_mask:0xf bank_mask:0xf
	v_add_f32_dpp v146, v146, v146 row_ror:2 row_mask:0xf bank_mask:0xf
	v_add_f32_dpp v147, v147, v147 row_ror:2 row_mask:0xf bank_mask:0xf
	v_add_f32_dpp v166, v166, v166 row_ror:2 row_mask:0xf bank_mask:0xf
	v_add_f32_dpp v140, v140, v140 row_ror:1 row_mask:0xf bank_mask:0xf
	v_add_f32_dpp v141, v141, v141 row_ror:1 row_mask:0xf bank_mask:0xf
	v_add_f32_dpp v142, v142, v142 row_ror:1 row_mask:0xf bank_mask:0xf
	v_add_f32_dpp v143, v143, v143 row_ror:1 row_mask:0xf bank_mask:0xf
	v_add_f32_dpp v144, v144, v144 row_ror:1 row_mask:0xf bank_mask:0xf
	v_add_f32_dpp v145, v145, v145 row_ror:1 row_mask:0xf bank_mask:0xf
	v_add_f32_dpp v146, v146, v146 row_ror:1 row_mask:0xf bank_mask:0xf
	v_add_f32_dpp v147, v147, v147 row_ror:1 row_mask:0xf bank_mask:0xf
	v_add_f32_dpp v166, v166, v166 row_ror:1 row_mask:0xf bank_mask:0xf
	v_cvt_pk_f16_f32 v252, v140, v141
	v_cvt_pk_f16_f32 v253, v142, v143
	v_cvt_pk_f16_f32 v254, v144, v145
	v_cvt_pk_f16_f32 v255, v146, v147
	s_waitcnt lgkmcnt(0)
	v_add_f32_e32 v209, s12, v166
	v_add_u32_e32 v220, s18, v102
	v_add_u32_e32 v220, s18, v220
	v_min_u32_e32 v218, s19, v220
	v_lshlrev_b32_e32 v218, 9, v218
	v_lshl_add_u64 v[216:217], v[222:223], 0, v[218:219]
	global_load_dword v228, v[216:217], off nt
	global_load_dword v229, v[216:217], off offset:128 nt
	global_load_dword v230, v[216:217], off offset:256 nt
	global_load_dword v231, v[216:217], off offset:384 nt
	v_add_u32_e32 v220, s18, v220
	v_min_u32_e32 v218, s19, v220
	v_lshlrev_b32_e32 v218, 9, v218
	v_lshl_add_u64 v[216:217], v[222:223], 0, v[218:219]
	global_load_dword v232, v[216:217], off nt
	global_load_dword v233, v[216:217], off offset:128 nt
	global_load_dword v234, v[216:217], off offset:256 nt
	global_load_dword v235, v[216:217], off offset:384 nt
	v_add_u32_e32 v220, s18, v220
	v_min_u32_e32 v218, s19, v220
	v_lshlrev_b32_e32 v218, 9, v218
	v_lshl_add_u64 v[216:217], v[222:223], 0, v[218:219]
	global_load_dword v236, v[216:217], off nt
	global_load_dword v237, v[216:217], off offset:128 nt
	global_load_dword v238, v[216:217], off offset:256 nt
	global_load_dword v239, v[216:217], off offset:384 nt
	v_add_u32_e32 v220, s18, v220
	v_min_u32_e32 v218, s19, v220
	v_lshlrev_b32_e32 v218, 9, v218
	v_lshl_add_u64 v[216:217], v[222:223], 0, v[218:219]
	global_load_dword v240, v[216:217], off nt
	global_load_dword v241, v[216:217], off offset:128 nt
	global_load_dword v242, v[216:217], off offset:256 nt
	global_load_dword v243, v[216:217], off offset:384 nt
	v_add_u32_e32 v220, s18, v220
	v_min_u32_e32 v218, s19, v220
	v_lshlrev_b32_e32 v218, 9, v218
	v_lshl_add_u64 v[216:217], v[222:223], 0, v[218:219]
	global_load_dword v244, v[216:217], off nt
	global_load_dword v245, v[216:217], off offset:128 nt
	global_load_dword v246, v[216:217], off offset:256 nt
	global_load_dword v247, v[216:217], off offset:384 nt
	v_add_u32_e32 v220, s18, v220
	v_min_u32_e32 v218, s19, v220
	v_lshlrev_b32_e32 v218, 9, v218
	v_lshl_add_u64 v[216:217], v[222:223], 0, v[218:219]
	global_load_dword v248, v[216:217], off nt
	global_load_dword v249, v[216:217], off offset:128 nt
	global_load_dword v250, v[216:217], off offset:256 nt
	global_load_dword v251, v[216:217], off offset:384 nt
	s_waitcnt vmcnt(24)

	.amdhsa_kernel _Z5k_decPKiPKDF16_S2_PKfS4_S4_Pf
		.amdhsa_group_segment_fixed_size 36864
		.amdhsa_private_segment_fixed_size 0
		.amdhsa_kernarg_size 312
		.amdhsa_user_sgpr_count 2
		.amdhsa_user_sgpr_dispatch_ptr 0
		.amdhsa_user_sgpr_queue_ptr 0
		.amdhsa_user_sgpr_kernarg_segment_ptr 1
		.amdhsa_user_sgpr_dispatch_id 0
		.amdhsa_user_sgpr_kernarg_preload_length 0
		.amdhsa_user_sgpr_kernarg_preload_offset 0
		.amdhsa_user_sgpr_private_segment_size 0
		.amdhsa_uses_dynamic_stack 0
		.amdhsa_enable_private_segment 0
		.amdhsa_system_sgpr_workgroup_id_x 1
		.amdhsa_system_sgpr_workgroup_id_y 0
		.amdhsa_system_sgpr_workgroup_id_z 0
		.amdhsa_system_sgpr_workgroup_info 0
		.amdhsa_system_vgpr_workitem_id 0
		.amdhsa_next_free_vgpr 256
		.amdhsa_next_free_sgpr 96
		.amdhsa_accum_offset 256
		.amdhsa_reserve_vcc 1
		.amdhsa_float_round_mode_32 0
		.amdhsa_float_round_mode_16_64 0
		.amdhsa_float_denorm_mode_32 3
		.amdhsa_float_denorm_mode_16_64 3
		.amdhsa_dx10_clamp 1
		.amdhsa_ieee_mode 1
		.amdhsa_fp16_overflow 0
		.amdhsa_tg_split 0
		.amdhsa_exception_fp_ieee_invalid_op 0
		.amdhsa_exception_fp_denorm_src 0
		.amdhsa_exception_fp_ieee_div_zero 0
		.amdhsa_exception_fp_ieee_overflow 0
		.amdhsa_exception_fp_ieee_underflow 0
		.amdhsa_exception_fp_ieee_inexact 0
		.amdhsa_exception_int_div_zero 0
	.end_amdhsa_kernel

amdhsa.kernels:
  - .agpr_count:     0
    .args:
      - .actual_access:  read_only
        .address_space:  global
        .offset:         0
        .size:           8
        .value_kind:     global_buffer
      - .actual_access:  read_only
        .address_space:  global
        .offset:         8
        .size:           8
        .value_kind:     global_buffer
      - .actual_access:  write_only
        .address_space:  global
        .offset:         16
        .size:           8
        .value_kind:     global_buffer
      - .actual_access:  read_only
        .address_space:  global
        .offset:         24
        .size:           8
        .value_kind:     global_buffer
      - .actual_access:  write_only
        .address_space:  global
        .offset:         32
        .size:           8
        .value_kind:     global_buffer
      - .actual_access:  write_only
        .address_space:  global
        .offset:         40
        .size:           8
        .value_kind:     global_buffer
      - .actual_access:  read_only
        .address_space:  global
        .offset:         48
        .size:           8
        .value_kind:     global_buffer
      - .actual_access:  read_only
        .address_space:  global
        .offset:         56
        .size:           8
        .value_kind:     global_buffer
      - .actual_access:  write_only
        .address_space:  global
        .offset:         64
        .size:           8
        .value_kind:     global_buffer
    .group_segment_fixed_size: 53904
    .kernarg_segment_align: 8
    .kernarg_segment_size: 72
    .language:       OpenCL C
    .language_version:
      - 2
      - 0
    .max_flat_workgroup_size: 1024
    .name:           _Z6k_partPKiS0_PiS1_PjS1_PKfS4_Pf
    .private_segment_fixed_size: 0
    .sgpr_count:     31
    .sgpr_spill_count: 0
    .symbol:         _Z6k_partPKiS0_PiS1_PjS1_PKfS4_Pf.kd
    .uniform_work_group_size: 1
    .uses_dynamic_stack: false
    .vgpr_count:     64
    .vgpr_spill_count: 0
    .wavefront_size: 64
  - .agpr_count:     0
    .args:
      - .actual_access:  read_only
        .address_space:  global
        .offset:         0
        .size:           8
        .value_kind:     global_buffer
      - .actual_access:  read_only
        .address_space:  global
        .offset:         8
        .size:           8
        .value_kind:     global_buffer
      - .actual_access:  read_only
        .address_space:  global
        .offset:         16
        .size:           8
        .value_kind:     global_buffer
      - .address_space:  global
        .offset:         24
        .size:           8
        .value_kind:     global_buffer
      - .actual_access:  read_only
        .address_space:  global
        .offset:         32
        .size:           8
        .value_kind:     global_buffer
      - .actual_access:  write_only
        .address_space:  global
        .offset:         40
        .size:           8
        .value_kind:     global_buffer
      - .actual_access:  write_only
        .address_space:  global
        .offset:         48
        .size:           8
        .value_kind:     global_buffer
      - .actual_access:  write_only
        .address_space:  global
        .offset:         56
        .size:           8
        .value_kind:     global_buffer
      - .actual_access:  write_only
        .address_space:  global
        .offset:         64
        .size:           8
        .value_kind:     global_buffer
      - .actual_access:  write_only
        .address_space:  global
        .offset:         72
        .size:           8
        .value_kind:     global_buffer
      - .actual_access:  read_only
        .address_space:  global
        .offset:         80
        .size:           8
        .value_kind:     global_buffer
      - .actual_access:  read_only
        .address_space:  global
        .offset:         88
        .size:           8
        .value_kind:     global_buffer
      - .actual_access:  read_only
        .address_space:  global
        .offset:         96
        .size:           8
        .value_kind:     global_buffer
      - .actual_access:  read_only
        .address_space:  global
        .offset:         104
        .size:           8
        .value_kind:     global_buffer
      - .actual_access:  write_only
        .address_space:  global
        .offset:         112
        .size:           8
        .value_kind:     global_buffer
      - .actual_access:  write_only
        .address_space:  global
        .offset:         120
        .size:           8
        .value_kind:     global_buffer
    .group_segment_fixed_size: 38940
    .kernarg_segment_align: 8
    .kernarg_segment_size: 128
    .language:       OpenCL C
    .language_version:
      - 2
      - 0
    .max_flat_workgroup_size: 1024
    .name:           _Z5k_csrPKjPKiS2_PiPKfPfPDF16_S3_S3_S3_S5_S5_S5_S5_S7_S6_
    .private_segment_fixed_size: 0
    .sgpr_count:     72
    .sgpr_spill_count: 0
    .symbol:         _Z5k_csrPKjPKiS2_PiPKfPfPDF16_S3_S3_S3_S5_S5_S5_S5_S7_S6_.kd
    .uniform_work_group_size: 1
    .uses_dynamic_stack: false
    .vgpr_count:     64
    .vgpr_spill_count: 0
    .wavefront_size: 64
  - .agpr_count:     0
    .args:
      - .actual_access:  read_only
        .address_space:  global
        .offset:         0
        .size:           8
        .value_kind:     global_buffer
      - .actual_access:  read_only
        .address_space:  global
        .offset:         8
        .size:           8
        .value_kind:     global_buffer
      - .actual_access:  read_only
        .address_space:  global
        .offset:         16
        .size:           8
        .value_kind:     global_buffer
      - .actual_access:  read_only
        .address_space:  global
        .offset:         24
        .size:           8
        .value_kind:     global_buffer
      - .actual_access:  read_only
        .address_space:  global
        .offset:         32
        .size:           8
        .value_kind:     global_buffer
      - .actual_access:  read_only
        .address_space:  global
        .offset:         40
        .size:           8
        .value_kind:     global_buffer
      - .actual_access:  write_only
        .address_space:  global
        .offset:         48
        .size:           8
        .value_kind:     global_buffer
      - .offset:         56
        .size:           4
        .value_kind:     hidden_block_count_x
      - .offset:         60
        .size:           4
        .value_kind:     hidden_block_count_y
      - .offset:         64
        .size:           4
        .value_kind:     hidden_block_count_z
      - .offset:         68
        .size:           2
        .value_kind:     hidden_group_size_x
      - .offset:         70
        .size:           2
        .value_kind:     hidden_group_size_y
      - .offset:         72
        .size:           2
        .value_kind:     hidden_group_size_z
      - .offset:         74
        .size:           2
        .value_kind:     hidden_remainder_x
      - .offset:         76
        .size:           2
        .value_kind:     hidden_remainder_y
      - .offset:         78
        .size:           2
        .value_kind:     hidden_remainder_z
      - .offset:         96
        .size:           8
        .value_kind:     hidden_global_offset_x
      - .offset:         104
        .size:           8
        .value_kind:     hidden_global_offset_y
      - .offset:         112
        .size:           8
        .value_kind:     hidden_global_offset_z
      - .offset:         120
        .size:           2
        .value_kind:     hidden_grid_dims
    .group_segment_fixed_size: 36864
    .kernarg_segment_align: 8
    .kernarg_segment_size: 312
    .language:       OpenCL C
    .language_version:
      - 2
      - 0
    .max_flat_workgroup_size: 256
    .name:           _Z5k_decPKiPKDF16_S2_PKfS4_S4_Pf
    .private_segment_fixed_size: 0
    .sgpr_count:     28
    .sgpr_spill_count: 0
    .symbol:         _Z5k_decPKiPKDF16_S2_PKfS4_S4_Pf.kd
    .uniform_work_group_size: 1
    .uses_dynamic_stack: false
    .vgpr_count:     256
    .vgpr_spill_count: 0
    .wavefront_size: 64
  - .agpr_count:     0
    .args:
      - .actual_access:  read_only
        .address_space:  global
        .offset:         0
        .size:           8
        .value_kind:     global_buffer
      - .actual_access:  read_only
        .address_space:  global
        .offset:         8
        .size:           8
        .value_kind:     global_buffer
      - .actual_access:  read_only
        .address_space:  global
        .offset:         16
        .size:           8
        .value_kind:     global_buffer
      - .actual_access:  read_only
        .address_space:  global
        .offset:         24
        .size:           8
        .value_kind:     global_buffer
      - .actual_access:  read_only
        .address_space:  global
        .offset:         32
        .size:           8
        .value_kind:     global_buffer
      - .actual_access:  read_only
        .address_space:  global
        .offset:         40
        .size:           8
        .value_kind:     global_buffer
      - .actual_access:  write_only
        .address_space:  global
        .offset:         48
        .size:           8
        .value_kind:     global_buffer
      - .actual_access:  read_only
        .address_space:  global
        .offset:         56
        .size:           8
        .value_kind:     global_buffer
    .group_segment_fixed_size: 0
    .kernarg_segment_align: 8
    .kernarg_segment_size: 64
    .language:       OpenCL C
    .language_version:
      - 2
      - 0
    .max_flat_workgroup_size: 64
    .name:           _Z5k_aggILi1EEvPKiS1_S1_PKDv4_jPKfS6_PS2_PDF16_
    .private_segment_fixed_size: 0
    .sgpr_count:     82
    .sgpr_spill_count: 0
    .symbol:         _Z5k_aggILi1EEvPKiS1_S1_PKDv4_jPKfS6_PS2_PDF16_.kd
    .uniform_work_group_size: 1
    .uses_dynamic_stack: false
    .vgpr_count:     72
    .vgpr_spill_count: 0
    .wavefront_size: 64
  - .agpr_count:     0
    .args:
      - .actual_access:  read_only
        .address_space:  global
        .offset:         0
        .size:           8
        .value_kind:     global_buffer
      - .actual_access:  read_only
        .address_space:  global
        .offset:         8
        .size:           8
        .value_kind:     global_buffer
      - .actual_access:  read_only
        .address_space:  global
        .offset:         16
        .size:           8
        .value_kind:     global_buffer
      - .actual_access:  read_only
        .address_space:  global
        .offset:         24
        .size:           8
        .value_kind:     global_buffer
      - .actual_access:  read_only
        .address_space:  global
        .offset:         32
        .size:           8
        .value_kind:     global_buffer
      - .actual_access:  read_only
        .address_space:  global
        .offset:         40
        .size:           8
        .value_kind:     global_buffer
      - .actual_access:  read_only
        .address_space:  global
        .offset:         48
        .size:           8
        .value_kind:     global_buffer
      - .actual_access:  write_only
        .address_space:  global
        .offset:         56
        .size:           8
        .value_kind:     global_buffer
    .group_segment_fixed_size: 0
    .kernarg_segment_align: 8
    .kernarg_segment_size: 64
    .language:       OpenCL C
    .language_version:
      - 2
      - 0
    .max_flat_workgroup_size: 64
    .name:           _Z5k_aggILi2EEvPKiS1_S1_PKDv4_jPKfS6_PS2_PDF16_
    .private_segment_fixed_size: 0
    .sgpr_count:     66
    .sgpr_spill_count: 0
    .symbol:         _Z5k_aggILi2EEvPKiS1_S1_PKDv4_jPKfS6_PS2_PDF16_.kd
    .uniform_work_group_size: 1
    .uses_dynamic_stack: false
    .vgpr_count:     72
    .vgpr_spill_count: 0
    .wavefront_size: 64
